# plus: rec1 W-fragment loads batched, prologue pe@w1 dot loop 4x batched (fewer serialized round trips), attention epilogue read-back loads batched
# speedup vs baseline: 1.2957x; 1.0041x over previous
; #define LAS __attribute__((address_space(3)))
; __device__ __forceinline__ unsigned pk2(float lo, float hi) { const pk2_f32x2 v = {lo, hi}; return __builtin_bit_cast(unsigned, __builtin_convertvector(v, pk2_bf16x2)); }
; __device__ __forceinline__ void rec1_unit(KArgs args, int L, int unit, LAS unsigned char* lds, int wave, int lane) {
;     ...
;     for (int f = 0; f < 16; ++f) { const int mat = f >> 3, n = (f >> 1) & 3, kk = f & 1; const float* W = mat ? Wx : Wa;
;         const int jout = 8 * (fr >> 2) + (fr & 3) + 4 * (n & 1) + 32 * (n >> 1); const float* wp = W + (32 * kk + 8 * q) * 64 + jout;
;         u32x4 w; w.x = pk2(wp[0], wp[64]); w.y = pk2(wp[128], wp[192]); w.z = pk2(wp[256], wp[320]); w.w = pk2(wp[384], wp[448]);
;         *(LAS u32x4*)(wl + f * 1024 + lane * 16) = w; }
.LBB0_175:
	v_add_lshl_u32 v4, v145, v144, 2
	v_mov_b32_e32 v5, v0
	s_add_u32 s14, s8, s16
	s_addc_u32 s15, s9, s17
	s_add_u32 s0, s14, 0x2000
	s_addc_u32 s1, s15, 0
	v_lshl_add_u64 v[6:7], s[14:15], 0, v[4:5]
	v_lshl_add_u64 v[8:9], s[0:1], 0, v[4:5]
	global_load_dword v10, v[6:7], off
	global_load_dword v11, v[6:7], off offset:256
	global_load_dword v12, v[6:7], off offset:512
	global_load_dword v13, v[6:7], off offset:768
	global_load_dword v14, v[6:7], off offset:1024
	global_load_dword v15, v[6:7], off offset:1280
	global_load_dword v16, v[6:7], off offset:1536
	global_load_dword v17, v[6:7], off offset:1792
	global_load_dword v18, v[8:9], off
	global_load_dword v19, v[8:9], off offset:256
	global_load_dword v20, v[8:9], off offset:512
	global_load_dword v21, v[8:9], off offset:768
	global_load_dword v22, v[8:9], off offset:1024
	global_load_dword v23, v[8:9], off offset:1280
	global_load_dword v24, v[8:9], off offset:1536
	global_load_dword v25, v[8:9], off offset:1792
	global_load_dword v26, v[6:7], off offset:16
	global_load_dword v27, v[6:7], off offset:272
	global_load_dword v28, v[6:7], off offset:528
	global_load_dword v29, v[6:7], off offset:784
	global_load_dword v30, v[6:7], off offset:1040
	global_load_dword v31, v[6:7], off offset:1296
	global_load_dword v32, v[6:7], off offset:1552
	global_load_dword v33, v[6:7], off offset:1808
	global_load_dword v34, v[8:9], off offset:16
	global_load_dword v35, v[8:9], off offset:272
	global_load_dword v36, v[8:9], off offset:528
	global_load_dword v37, v[8:9], off offset:784
	global_load_dword v38, v[8:9], off offset:1040
	global_load_dword v39, v[8:9], off offset:1296
	global_load_dword v40, v[8:9], off offset:1552
	global_load_dword v41, v[8:9], off offset:1808
	global_load_dword v42, v[6:7], off offset:128
	global_load_dword v43, v[6:7], off offset:384
	global_load_dword v44, v[6:7], off offset:640
	global_load_dword v45, v[6:7], off offset:896
	global_load_dword v46, v[6:7], off offset:1152
	global_load_dword v47, v[6:7], off offset:1408
	global_load_dword v48, v[6:7], off offset:1664
	global_load_dword v49, v[6:7], off offset:1920
	global_load_dword v50, v[8:9], off offset:128
	global_load_dword v51, v[8:9], off offset:384
	global_load_dword v52, v[8:9], off offset:640
	global_load_dword v53, v[8:9], off offset:896
	global_load_dword v54, v[8:9], off offset:1152
	global_load_dword v55, v[8:9], off offset:1408
	global_load_dword v56, v[8:9], off offset:1664
	global_load_dword v57, v[8:9], off offset:1920
	global_load_dword v58, v[6:7], off offset:144
	global_load_dword v59, v[6:7], off offset:400
	global_load_dword v60, v[6:7], off offset:656
	global_load_dword v61, v[6:7], off offset:912
	global_load_dword v62, v[6:7], off offset:1168
	global_load_dword v63, v[6:7], off offset:1424
	global_load_dword v64, v[6:7], off offset:1680
	global_load_dword v65, v[6:7], off offset:1936
	global_load_dword v66, v[8:9], off offset:144
	global_load_dword v67, v[8:9], off offset:400
	global_load_dword v68, v[8:9], off offset:656
	global_load_dword v69, v[8:9], off offset:912
	global_load_dword v70, v[8:9], off offset:1168
	global_load_dword v71, v[8:9], off offset:1424
	global_load_dword v72, v[8:9], off offset:1680
	global_load_dword v73, v[8:9], off offset:1936
	s_waitcnt vmcnt(0)
	v_cvt_pk_bf16_f32 v10, v10, v11
	v_cvt_pk_bf16_f32 v11, v12, v13
	v_cvt_pk_bf16_f32 v12, v14, v15
	v_cvt_pk_bf16_f32 v13, v16, v17
	ds_write_b128 v146, v[10:13]
	v_cvt_pk_bf16_f32 v18, v18, v19
	v_cvt_pk_bf16_f32 v19, v20, v21
	v_cvt_pk_bf16_f32 v20, v22, v23
	v_cvt_pk_bf16_f32 v21, v24, v25
	ds_write_b128 v146, v[18:21] offset:1024
	v_cvt_pk_bf16_f32 v26, v26, v27
	v_cvt_pk_bf16_f32 v27, v28, v29
	v_cvt_pk_bf16_f32 v28, v30, v31
	v_cvt_pk_bf16_f32 v29, v32, v33
	ds_write_b128 v146, v[26:29] offset:2048
	v_cvt_pk_bf16_f32 v34, v34, v35
	v_cvt_pk_bf16_f32 v35, v36, v37
	v_cvt_pk_bf16_f32 v36, v38, v39
	v_cvt_pk_bf16_f32 v37, v40, v41
	ds_write_b128 v146, v[34:37] offset:3072
	v_cvt_pk_bf16_f32 v42, v42, v43
	v_cvt_pk_bf16_f32 v43, v44, v45
	v_cvt_pk_bf16_f32 v44, v46, v47
	v_cvt_pk_bf16_f32 v45, v48, v49
	ds_write_b128 v146, v[42:45] offset:4096
	v_cvt_pk_bf16_f32 v50, v50, v51
	v_cvt_pk_bf16_f32 v51, v52, v53
	v_cvt_pk_bf16_f32 v52, v54, v55
	v_cvt_pk_bf16_f32 v53, v56, v57
	ds_write_b128 v146, v[50:53] offset:5120
	v_cvt_pk_bf16_f32 v58, v58, v59
	v_cvt_pk_bf16_f32 v59, v60, v61
	v_cvt_pk_bf16_f32 v60, v62, v63
	v_cvt_pk_bf16_f32 v61, v64, v65
	ds_write_b128 v146, v[58:61] offset:6144
	v_cvt_pk_bf16_f32 v66, v66, v67
	v_cvt_pk_bf16_f32 v67, v68, v69
	v_cvt_pk_bf16_f32 v68, v70, v71
	v_cvt_pk_bf16_f32 v69, v72, v73
	ds_write_b128 v146, v[66:69] offset:7168
	s_add_u32 s14, s12, s16
	s_addc_u32 s15, s13, s17
	s_add_u32 s0, s14, 0x2000
	s_addc_u32 s1, s15, 0
	v_lshl_add_u64 v[6:7], s[14:15], 0, v[4:5]
	v_lshl_add_u64 v[8:9], s[0:1], 0, v[4:5]
	s_waitcnt lgkmcnt(0)
; #define LAS __attribute__((address_space(3)))
; #define LDS_WAIT() asm volatile("s_waitcnt lgkmcnt(0)" ::: "memory")
; __device__ __forceinline__ unsigned pk2(float lo, float hi) { const pk2_f32x2 v = {lo, hi}; return __builtin_bit_cast(unsigned, __builtin_convertvector(v, pk2_bf16x2)); }
; #define REC_LOAD_TILE(dst_, tile_) do { const int t_ = t0 + (tile_) * 16 + fr; _Pragma("unroll") for (int kk_ = 0; kk_ < 2; ++kk_) _Pragma("unroll") for (int j_ = 0; j_ < 4; ++j_) { const int tt_ = t_ - 3 + j_; \
;         dst_[kk_][j_] = *(const u32x4*)(zb + (size_t)(tt_ > 0 ? tt_ : 0) * ZP + 32 * kk_ + 8 * q); } } while (0)
; __device__ __forceinline__ void rec1_unit(KArgs args, int L, int unit, LAS unsigned char* lds, int wave, int lane) {
;     ...
;     for (int f = 0; f < 16; ++f) { const int mat = f >> 3, n = (f >> 1) & 3, kk = f & 1; const float* W = mat ? Wx : Wa;
;         const int jout = 8 * (fr >> 2) + (fr & 3) + 4 * (n & 1) + 32 * (n >> 1); const float* wp = W + (32 * kk + 8 * q) * 64 + jout;
;         u32x4 w; w.x = pk2(wp[0], wp[64]); w.y = pk2(wp[128], wp[192]); w.z = pk2(wp[256], wp[320]); w.w = pk2(wp[384], wp[448]);
;         *(LAS u32x4*)(wl + f * 1024 + lane * 16) = w; }
;     LAS float* ct = (LAS float*)(lds + 131072 + wave * 2048);
;     { const int c = 64 * hb + lane; const float* cw = args->in[I_CONVW] + (size_t)L * 4 * 512;
;       ct[lane * 8 + 0] = cw[c]; ct[lane * 8 + 1] = cw[512 + c]; ct[lane * 8 + 2] = cw[1024 + c]; ct[lane * 8 + 3] = cw[1536 + c];
;       ct[lane * 8 + 4] = args->in[I_CONVB][L * 512 + c]; ct[lane * 8 + 5] = args->in[I_BA][L * 512 + c]; ct[lane * 8 + 6] = args->in[I_BX][L * 512 + c];
;       ct[lane * 8 + 7] = ((const float*)(ws + WS_C8))[L * 512 + c]; }
;     LDS_WAIT();
;     float Acar[2][8], Hcar[2][8];
; #pragma unroll
;     for (int kk = 0; kk < 2; ++kk)
; #pragma unroll
;         for (int e = 0; e < 8; ++e) { Acar[kk][e] = 1.f; Hcar[kk][e] = 0.f; }
;     const bf16* zb = z + (size_t)(b * SEQ) * ZP + ZC_XR + 64 * hb;
;     const int bidx15 = ((lane & ~15) | 15) << 2;
;     u32x4 rawc[2][4];
;     ...
;     REC_LOAD_TILE(rawc, 0);
	global_load_dword v10, v[6:7], off
	global_load_dword v11, v[6:7], off offset:256
	global_load_dword v12, v[6:7], off offset:512
	global_load_dword v13, v[6:7], off offset:768
	global_load_dword v14, v[6:7], off offset:1024
	global_load_dword v15, v[6:7], off offset:1280
	global_load_dword v16, v[6:7], off offset:1536
	global_load_dword v17, v[6:7], off offset:1792
	global_load_dword v18, v[8:9], off
	global_load_dword v19, v[8:9], off offset:256
	global_load_dword v20, v[8:9], off offset:512
	global_load_dword v21, v[8:9], off offset:768
	global_load_dword v22, v[8:9], off offset:1024
	global_load_dword v23, v[8:9], off offset:1280
	global_load_dword v24, v[8:9], off offset:1536
	global_load_dword v25, v[8:9], off offset:1792
	global_load_dword v26, v[6:7], off offset:16
	global_load_dword v27, v[6:7], off offset:272
	global_load_dword v28, v[6:7], off offset:528
	global_load_dword v29, v[6:7], off offset:784
	global_load_dword v30, v[6:7], off offset:1040
	global_load_dword v31, v[6:7], off offset:1296
	global_load_dword v32, v[6:7], off offset:1552
	global_load_dword v33, v[6:7], off offset:1808
	global_load_dword v34, v[8:9], off offset:16
	global_load_dword v35, v[8:9], off offset:272
	global_load_dword v36, v[8:9], off offset:528
	global_load_dword v37, v[8:9], off offset:784
	global_load_dword v38, v[8:9], off offset:1040
	global_load_dword v39, v[8:9], off offset:1296
	global_load_dword v40, v[8:9], off offset:1552
	global_load_dword v41, v[8:9], off offset:1808
	global_load_dword v42, v[6:7], off offset:128
	global_load_dword v43, v[6:7], off offset:384
	global_load_dword v44, v[6:7], off offset:640
	global_load_dword v45, v[6:7], off offset:896
	global_load_dword v46, v[6:7], off offset:1152
	global_load_dword v47, v[6:7], off offset:1408
	global_load_dword v48, v[6:7], off offset:1664
	global_load_dword v49, v[6:7], off offset:1920
	global_load_dword v50, v[8:9], off offset:128
	global_load_dword v51, v[8:9], off offset:384
	global_load_dword v52, v[8:9], off offset:640
	global_load_dword v53, v[8:9], off offset:896
	global_load_dword v54, v[8:9], off offset:1152
	global_load_dword v55, v[8:9], off offset:1408
	global_load_dword v56, v[8:9], off offset:1664
	global_load_dword v57, v[8:9], off offset:1920
	global_load_dword v58, v[6:7], off offset:144
	global_load_dword v59, v[6:7], off offset:400
	global_load_dword v60, v[6:7], off offset:656
	global_load_dword v61, v[6:7], off offset:912
	global_load_dword v62, v[6:7], off offset:1168
	global_load_dword v63, v[6:7], off offset:1424
	global_load_dword v64, v[6:7], off offset:1680
	global_load_dword v65, v[6:7], off offset:1936
	global_load_dword v66, v[8:9], off offset:144
	global_load_dword v67, v[8:9], off offset:400
	global_load_dword v68, v[8:9], off offset:656
	global_load_dword v69, v[8:9], off offset:912
	global_load_dword v70, v[8:9], off offset:1168
	global_load_dword v71, v[8:9], off offset:1424
	global_load_dword v72, v[8:9], off offset:1680
	global_load_dword v73, v[8:9], off offset:1936
	s_waitcnt vmcnt(0)
	v_cvt_pk_bf16_f32 v10, v10, v11
	v_cvt_pk_bf16_f32 v11, v12, v13
	v_cvt_pk_bf16_f32 v12, v14, v15
	v_cvt_pk_bf16_f32 v13, v16, v17
	ds_write_b128 v146, v[10:13] offset:8192
	v_cvt_pk_bf16_f32 v18, v18, v19
	v_cvt_pk_bf16_f32 v19, v20, v21
	v_cvt_pk_bf16_f32 v20, v22, v23
	v_cvt_pk_bf16_f32 v21, v24, v25
	ds_write_b128 v146, v[18:21] offset:9216
	v_cvt_pk_bf16_f32 v26, v26, v27
	v_cvt_pk_bf16_f32 v27, v28, v29
	v_cvt_pk_bf16_f32 v28, v30, v31
	v_cvt_pk_bf16_f32 v29, v32, v33
	ds_write_b128 v146, v[26:29] offset:10240
	v_cvt_pk_bf16_f32 v34, v34, v35
	v_cvt_pk_bf16_f32 v35, v36, v37
	v_cvt_pk_bf16_f32 v36, v38, v39
	v_cvt_pk_bf16_f32 v37, v40, v41
	ds_write_b128 v146, v[34:37] offset:11264
	v_cvt_pk_bf16_f32 v42, v42, v43
	v_cvt_pk_bf16_f32 v43, v44, v45
	v_cvt_pk_bf16_f32 v44, v46, v47
	v_cvt_pk_bf16_f32 v45, v48, v49
	ds_write_b128 v146, v[42:45] offset:12288
	v_cvt_pk_bf16_f32 v50, v50, v51
	v_cvt_pk_bf16_f32 v51, v52, v53
	v_cvt_pk_bf16_f32 v52, v54, v55
	v_cvt_pk_bf16_f32 v53, v56, v57
	ds_write_b128 v146, v[50:53] offset:13312
	v_cvt_pk_bf16_f32 v58, v58, v59
	v_cvt_pk_bf16_f32 v59, v60, v61
	v_cvt_pk_bf16_f32 v60, v62, v63
	v_cvt_pk_bf16_f32 v61, v64, v65
	ds_write_b128 v146, v[58:61] offset:14336
	v_cvt_pk_bf16_f32 v66, v66, v67
	v_cvt_pk_bf16_f32 v67, v68, v69
	v_cvt_pk_bf16_f32 v68, v70, v71
	v_cvt_pk_bf16_f32 v69, v72, v73
	ds_write_b128 v146, v[66:69] offset:15360
	global_load_dword v4, v[100:101], off
	global_load_dword v5, v[100:101], off offset:2048
	global_load_dword v6, v[102:103], off
	global_load_dword v7, v[104:105], off
	global_load_dword v8, v[106:107], off
	global_load_dword v9, v[108:109], off
	global_load_dword v10, v[110:111], off
	global_load_dword v11, v[112:113], off
	s_lshl_b32 s0, s10, 8
	s_and_b32 s4, s0, 0xf00
	s_and_b32 s0, s0, 0xfffff000
	v_add_u32_e32 v152, s4, v148
	v_mad_i64_i32 v[2:3], s[0:1], s0, v209, v[114:115]
	v_or_b32_e32 v12, s4, v147
	v_max_i32_e32 v14, 0, v152
	v_max_i32_e32 v16, -1, v152
	v_max_i32_e32 v17, -2, v152
	v_mov_b32_e32 v13, v0
	v_mul_u32_u24_e32 v12, 0x1400, v12
	v_mad_u64_u32 v[14:15], s[0:1], v14, s88, v[2:3]
	v_add_u32_e32 v16, 1, v16
	v_add_u32_e32 v18, 2, v17
	v_lshl_add_u64 v[12:13], v[2:3], 0, v[12:13]
	v_mad_u64_u32 v[16:17], s[0:1], v16, s88, v[2:3]
	v_mad_u64_u32 v[18:19], s[0:1], v18, s88, v[2:3]
	s_and_b32 s11, s27, 0xf00
	s_and_b32 s0, s27, 0xfffff000
	v_or_b32_e32 v153, s11, v147
	s_waitcnt lgkmcnt(3)
	v_mov_b32_e32 v116, 0
	v_or_b32_e32 v154, s0, v153
	s_mov_b32 s29, 16
	v_mov_b32_e32 v117, v116
	v_mov_b32_e32 v118, v116
	v_mov_b32_e32 v119, v116
	v_mov_b32_e32 v120, v116
	v_mov_b32_e32 v121, v116
	v_mov_b32_e32 v122, v116
	v_mov_b32_e32 v123, v116
	v_mov_b32_e32 v128, v116
	v_mov_b32_e32 v129, v116
	v_mov_b32_e32 v134, v116
	v_mov_b32_e32 v135, v116
	v_mov_b32_e32 v138, v116
	v_mov_b32_e32 v139, v116
	s_waitcnt vmcnt(4)
	ds_write_b128 v151, v[4:7]
	s_waitcnt vmcnt(0)
	ds_write_b128 v151, v[8:11] offset:16
	s_waitcnt lgkmcnt(0)
	global_load_dwordx4 v[74:77], v[14:15], off
	global_load_dwordx4 v[58:61], v[14:15], off offset:64
	global_load_dwordx4 v[70:73], v[16:17], off
	global_load_dwordx4 v[54:57], v[16:17], off offset:64
	global_load_dwordx4 v[66:69], v[18:19], off
	global_load_dwordx4 v[50:53], v[18:19], off offset:64
	global_load_dwordx4 v[62:65], v[12:13], off
	global_load_dwordx4 v[46:49], v[12:13], off offset:64
	v_mov_b32_e32 v4, 1.0
	v_mov_b32_e32 v5, v4
	v_mov_b32_e32 v8, v4
	v_mov_b32_e32 v9, v4
	v_mov_b32_e32 v12, v4
	v_mov_b32_e32 v13, v4
	v_mov_b32_e32 v6, v116
	v_mov_b32_e32 v7, v116
	v_mov_b32_e32 v136, v4
	v_mov_b32_e32 v137, v4
	v_mov_b32_e32 v132, v4
	v_mov_b32_e32 v133, v4
	v_mov_b32_e32 v130, v4
	v_mov_b32_e32 v131, v4
	v_mov_b32_e32 v126, v4
	v_mov_b32_e32 v127, v4
	s_waitcnt lgkmcnt(4)
	v_mov_b32_e32 v124, v4
	s_waitcnt lgkmcnt(3)
	v_mov_b32_e32 v125, v4

; __device__ __forceinline__ unsigned cvtpk(float lo, float hi) { f32x2_t v = {lo, hi}; bf16x2_t b = __builtin_convertvector(v, bf16x2_t); return __builtin_bit_cast(unsigned, b); }
; __device__ __forceinline__ void att_unit_mfma(KArgs args, int b, int qb, LAS unsigned char* lds, int wave0, int lane0, int tid0) {
;     ...
;     ATT_IDS
;     float tot = 0.f;
; #pragma unroll
;     for (int h2 = 0; h2 < 8; ++h2) tot += red[h2 * 64 + tl];
;     const float rstd = rsqrtf(tot * (1.f / 512.f) + EPS);
;     { bf16* orow = mixed + (size_t)tok * DM + 512 + (4 + r) * 64;
; #pragma unroll
;       for (int dt = 0; dt < 2; ++dt)
; #pragma unroll
;           for (int q4 = 0; q4 < 4; ++q4) { u32x2 w; const unsigned p0 = OUTP[8 * dt + 2 * q4], p1 = OUTP[8 * dt + 2 * q4 + 1];
;               w.x = cvtpk(bflo(p0) * rstd, bfhi(p0) * rstd); w.y = cvtpk(bflo(p1) * rstd, bfhi(p1) * rstd);
;               *(u32x2*)(orow + 32 * dt + 8 * q4 + 4 * h) = w; } }
;     { bf16* orow = mixed + (size_t)tok * DM + 512 + r * 64;
; #pragma unroll
;       for (int dt = 0; dt < 2; ++dt)
; #pragma unroll
;           for (int q4 = 0; q4 < 4; ++q4) { u32x2 w = *(const u32x2*)(orow + 32 * dt + 8 * q4 + 4 * h);
;               w.x = cvtpk(bflo(w.x) * rstd, bfhi(w.x) * rstd); w.y = cvtpk(bflo(w.y) * rstd, bfhi(w.y) * rstd);
;               *(u32x2*)(orow + 32 * dt + 8 * q4 + 4 * h) = w; } }
.LBB0_532:
	v_mov_b32_e32 v1, v174
	s_mov_b32 s0, s69
	s_lshl_b32 s0, s0, 5
	v_and_b32_e32 v2, 31, v1
	v_and_or_b32 v4, s0, 32, v2
	v_lshl_add_u32 v2, v4, 2, 0
	v_add_u32_e32 v5, 0x24740, v2
	ds_read2st64_b32 v[2:3], v5 offset1:1
	s_mov_b32 s79, 0x800000
	v_or_b32_e32 v4, s94, v4
	v_readlane_b32 s2, v255, 21
	v_readlane_b32 s3, v255, 22
	s_waitcnt lgkmcnt(0)
	v_add_f32_e32 v2, 0, v2
	v_add_f32_e32 v6, v2, v3
	ds_read2st64_b32 v[2:3], v5 offset0:2 offset1:3
	s_andn2_b32 s0, s0, 63
	v_ashrrev_i32_e32 v1, 3, v1
	s_ashr_i32 s1, s0, 31
	v_lshlrev_b32_e32 v8, 16, v161
	s_waitcnt lgkmcnt(0)
	v_add_f32_e32 v2, v6, v2
	v_add_f32_e32 v6, v2, v3
	ds_read2st64_b32 v[2:3], v5 offset0:4 offset1:5
	v_and_b32_e32 v9, 0xffff0000, v161
	s_waitcnt lgkmcnt(0)
	v_add_f32_e32 v2, v6, v2
	v_add_f32_e32 v6, v2, v3
	ds_read2st64_b32 v[2:3], v5 offset0:6 offset1:7
	v_ashrrev_i32_e32 v5, 31, v4
	v_lshlrev_b64 v[4:5], 11, v[4:5]
	v_lshl_add_u64 v[4:5], s[2:3], 0, v[4:5]
	v_lshl_add_u64 v[4:5], s[0:1], 1, v[4:5]
	s_waitcnt lgkmcnt(0)
	v_add_f32_e32 v2, v6, v2
	v_add_f32_e32 v2, v2, v3
	v_fmamk_f32 v2, v2, 0x3b000000, v206
	v_cmp_gt_f32_e32 vcc, s79, v2
	v_mul_f32_e32 v3, 0x4b800000, v2
	v_and_b32_e32 v6, -4, v1
	v_cndmask_b32_e32 v2, v2, v3, vcc
	v_rsq_f32_e32 v2, v2
	v_ashrrev_i32_e32 v7, 31, v6
	v_lshl_add_u64 v[4:5], v[6:7], 1, v[4:5]
	global_load_dwordx2 v[10:11], v[4:5], off offset:1024
	global_load_dwordx2 v[12:13], v[4:5], off offset:1040
	global_load_dwordx2 v[14:15], v[4:5], off offset:1056
	global_load_dwordx2 v[16:17], v[4:5], off offset:1072
	global_load_dwordx2 v[18:19], v[4:5], off offset:1088
	global_load_dwordx2 v[20:21], v[4:5], off offset:1104
	global_load_dwordx2 v[22:23], v[4:5], off offset:1120
	global_load_dwordx2 v[24:25], v[4:5], off offset:1136
	v_lshlrev_b32_e32 v6, 16, v160
	v_mul_f32_e32 v3, 0x45800000, v2
	v_cndmask_b32_e32 v2, v2, v3, vcc
	v_and_b32_e32 v7, 0xffff0000, v160
	v_pk_mul_f32 v[6:7], v[2:3], v[6:7] op_sel_hi:[0,1]
	v_pk_mul_f32 v[8:9], v[2:3], v[8:9] op_sel_hi:[0,1]
	v_cvt_pk_bf16_f32 v6, v6, v7
	v_cvt_pk_bf16_f32 v7, v8, v9
	global_store_dwordx2 v[4:5], v[6:7], off offset:1536
	v_lshlrev_b32_e32 v6, 16, v148
	v_and_b32_e32 v7, 0xffff0000, v148
	v_lshlrev_b32_e32 v8, 16, v149
	v_and_b32_e32 v9, 0xffff0000, v149
	v_pk_mul_f32 v[6:7], v[2:3], v[6:7] op_sel_hi:[0,1]
	v_pk_mul_f32 v[8:9], v[2:3], v[8:9] op_sel_hi:[0,1]
	v_cvt_pk_bf16_f32 v6, v6, v7
	v_cvt_pk_bf16_f32 v7, v8, v9
	global_store_dwordx2 v[4:5], v[6:7], off offset:1552
	v_lshlrev_b32_e32 v6, 16, v158
	v_and_b32_e32 v7, 0xffff0000, v158
	v_lshlrev_b32_e32 v8, 16, v159
	v_and_b32_e32 v9, 0xffff0000, v159
	v_pk_mul_f32 v[6:7], v[2:3], v[6:7] op_sel_hi:[0,1]
	v_pk_mul_f32 v[8:9], v[2:3], v[8:9] op_sel_hi:[0,1]
	v_cvt_pk_bf16_f32 v6, v6, v7
	v_cvt_pk_bf16_f32 v7, v8, v9
	global_store_dwordx2 v[4:5], v[6:7], off offset:1568
	v_lshlrev_b32_e32 v6, 16, v162
	v_and_b32_e32 v7, 0xffff0000, v162
	v_lshlrev_b32_e32 v8, 16, v163
	v_and_b32_e32 v9, 0xffff0000, v163
	v_pk_mul_f32 v[6:7], v[2:3], v[6:7] op_sel_hi:[0,1]
	v_pk_mul_f32 v[8:9], v[2:3], v[8:9] op_sel_hi:[0,1]
	v_cvt_pk_bf16_f32 v6, v6, v7
	v_cvt_pk_bf16_f32 v7, v8, v9
	global_store_dwordx2 v[4:5], v[6:7], off offset:1584
	v_lshlrev_b32_e32 v6, 16, v150
	v_and_b32_e32 v7, 0xffff0000, v150
	v_lshlrev_b32_e32 v8, 16, v151
	v_and_b32_e32 v9, 0xffff0000, v151
	v_pk_mul_f32 v[6:7], v[2:3], v[6:7] op_sel_hi:[0,1]
	v_pk_mul_f32 v[8:9], v[2:3], v[8:9] op_sel_hi:[0,1]
	v_cvt_pk_bf16_f32 v6, v6, v7
	v_cvt_pk_bf16_f32 v7, v8, v9
	global_store_dwordx2 v[4:5], v[6:7], off offset:1600
	v_lshlrev_b32_e32 v6, 16, v152
	v_and_b32_e32 v7, 0xffff0000, v152
	v_lshlrev_b32_e32 v8, 16, v153
	v_and_b32_e32 v9, 0xffff0000, v153
	v_pk_mul_f32 v[6:7], v[2:3], v[6:7] op_sel_hi:[0,1]
	v_pk_mul_f32 v[8:9], v[2:3], v[8:9] op_sel_hi:[0,1]
	v_cvt_pk_bf16_f32 v6, v6, v7
	v_cvt_pk_bf16_f32 v7, v8, v9
	global_store_dwordx2 v[4:5], v[6:7], off offset:1616
	v_lshlrev_b32_e32 v6, 16, v154
	v_and_b32_e32 v7, 0xffff0000, v154
	v_lshlrev_b32_e32 v8, 16, v155
	v_and_b32_e32 v9, 0xffff0000, v155
	v_pk_mul_f32 v[6:7], v[2:3], v[6:7] op_sel_hi:[0,1]
	v_pk_mul_f32 v[8:9], v[2:3], v[8:9] op_sel_hi:[0,1]
	v_cvt_pk_bf16_f32 v6, v6, v7
	v_cvt_pk_bf16_f32 v7, v8, v9
	global_store_dwordx2 v[4:5], v[6:7], off offset:1632
	v_lshlrev_b32_e32 v6, 16, v156
	v_and_b32_e32 v7, 0xffff0000, v156
	v_lshlrev_b32_e32 v8, 16, v157
	v_and_b32_e32 v9, 0xffff0000, v157
	v_pk_mul_f32 v[6:7], v[2:3], v[6:7] op_sel_hi:[0,1]
	v_pk_mul_f32 v[8:9], v[2:3], v[8:9] op_sel_hi:[0,1]
	v_cvt_pk_bf16_f32 v6, v6, v7
	v_cvt_pk_bf16_f32 v7, v8, v9
	global_store_dwordx2 v[4:5], v[6:7], off offset:1648
	v_readlane_b32 s2, v255, 25
	s_add_i32 s2, s2, 1
	s_cmp_eq_u32 s2, 4
	s_waitcnt vmcnt(8)
; __device__ __forceinline__ unsigned cvtpk(float lo, float hi) { f32x2_t v = {lo, hi}; bf16x2_t b = __builtin_convertvector(v, bf16x2_t); return __builtin_bit_cast(unsigned, b); }
; __device__ __forceinline__ void att_unit_mfma(KArgs args, int b, int qb, LAS unsigned char* lds, int wave0, int lane0, int tid0) {
;     ...
;     { bf16* orow = mixed + (size_t)tok * DM + 512 + r * 64;
; #pragma unroll
;       for (int dt = 0; dt < 2; ++dt)
; #pragma unroll
;           for (int q4 = 0; q4 < 4; ++q4) { u32x2 w = *(const u32x2*)(orow + 32 * dt + 8 * q4 + 4 * h);
;               w.x = cvtpk(bflo(w.x) * rstd, bfhi(w.x) * rstd); w.y = cvtpk(bflo(w.y) * rstd, bfhi(w.y) * rstd);
;               *(u32x2*)(orow + 32 * dt + 8 * q4 + 4 * h) = w; } }
;     __syncthreads();
	v_lshlrev_b32_e32 v8, 16, v10
	v_and_b32_e32 v9, 0xffff0000, v10
	v_pk_mul_f32 v[8:9], v[2:3], v[8:9] op_sel_hi:[0,1]
	v_cvt_pk_bf16_f32 v6, v8, v9
	v_lshlrev_b32_e32 v8, 16, v11
	v_and_b32_e32 v9, 0xffff0000, v11
	v_pk_mul_f32 v[8:9], v[2:3], v[8:9] op_sel_hi:[0,1]
	v_cvt_pk_bf16_f32 v7, v8, v9
	global_store_dwordx2 v[4:5], v[6:7], off offset:1024
	v_lshlrev_b32_e32 v8, 16, v12
	v_and_b32_e32 v9, 0xffff0000, v12
	v_pk_mul_f32 v[8:9], v[2:3], v[8:9] op_sel_hi:[0,1]
	v_cvt_pk_bf16_f32 v6, v8, v9
	v_lshlrev_b32_e32 v8, 16, v13
	v_and_b32_e32 v9, 0xffff0000, v13
	v_pk_mul_f32 v[8:9], v[2:3], v[8:9] op_sel_hi:[0,1]
	v_cvt_pk_bf16_f32 v7, v8, v9
	global_store_dwordx2 v[4:5], v[6:7], off offset:1040
	v_lshlrev_b32_e32 v8, 16, v14
	v_and_b32_e32 v9, 0xffff0000, v14
	v_pk_mul_f32 v[8:9], v[2:3], v[8:9] op_sel_hi:[0,1]
	v_cvt_pk_bf16_f32 v6, v8, v9
	v_lshlrev_b32_e32 v8, 16, v15
	v_and_b32_e32 v9, 0xffff0000, v15
	v_pk_mul_f32 v[8:9], v[2:3], v[8:9] op_sel_hi:[0,1]
	v_cvt_pk_bf16_f32 v7, v8, v9
	global_store_dwordx2 v[4:5], v[6:7], off offset:1056
	v_lshlrev_b32_e32 v8, 16, v16
	v_and_b32_e32 v9, 0xffff0000, v16
	v_pk_mul_f32 v[8:9], v[2:3], v[8:9] op_sel_hi:[0,1]
	v_cvt_pk_bf16_f32 v6, v8, v9
	v_lshlrev_b32_e32 v8, 16, v17
	v_and_b32_e32 v9, 0xffff0000, v17
	v_pk_mul_f32 v[8:9], v[2:3], v[8:9] op_sel_hi:[0,1]
	v_cvt_pk_bf16_f32 v7, v8, v9
	global_store_dwordx2 v[4:5], v[6:7], off offset:1072
	v_lshlrev_b32_e32 v8, 16, v18
	v_and_b32_e32 v9, 0xffff0000, v18
	v_pk_mul_f32 v[8:9], v[2:3], v[8:9] op_sel_hi:[0,1]
	v_cvt_pk_bf16_f32 v6, v8, v9
	v_lshlrev_b32_e32 v8, 16, v19
	v_and_b32_e32 v9, 0xffff0000, v19
	v_pk_mul_f32 v[8:9], v[2:3], v[8:9] op_sel_hi:[0,1]
	v_cvt_pk_bf16_f32 v7, v8, v9
	global_store_dwordx2 v[4:5], v[6:7], off offset:1088
	v_lshlrev_b32_e32 v8, 16, v20
	v_and_b32_e32 v9, 0xffff0000, v20
	v_pk_mul_f32 v[8:9], v[2:3], v[8:9] op_sel_hi:[0,1]
	v_cvt_pk_bf16_f32 v6, v8, v9
	v_lshlrev_b32_e32 v8, 16, v21
	v_and_b32_e32 v9, 0xffff0000, v21
	v_pk_mul_f32 v[8:9], v[2:3], v[8:9] op_sel_hi:[0,1]
	v_cvt_pk_bf16_f32 v7, v8, v9
	global_store_dwordx2 v[4:5], v[6:7], off offset:1104
	v_lshlrev_b32_e32 v8, 16, v22
	v_and_b32_e32 v9, 0xffff0000, v22
	v_pk_mul_f32 v[8:9], v[2:3], v[8:9] op_sel_hi:[0,1]
	v_cvt_pk_bf16_f32 v6, v8, v9
	v_lshlrev_b32_e32 v8, 16, v23
	v_and_b32_e32 v9, 0xffff0000, v23
	v_pk_mul_f32 v[8:9], v[2:3], v[8:9] op_sel_hi:[0,1]
	v_cvt_pk_bf16_f32 v7, v8, v9
	global_store_dwordx2 v[4:5], v[6:7], off offset:1120
	v_lshlrev_b32_e32 v8, 16, v24
	v_and_b32_e32 v9, 0xffff0000, v24
	v_pk_mul_f32 v[8:9], v[2:3], v[8:9] op_sel_hi:[0,1]
	v_cvt_pk_bf16_f32 v6, v8, v9
	v_lshlrev_b32_e32 v8, 16, v25
	v_and_b32_e32 v9, 0xffff0000, v25
	v_pk_mul_f32 v[2:3], v[2:3], v[8:9] op_sel_hi:[0,1]
	v_cvt_pk_bf16_f32 v7, v2, v3
	global_store_dwordx2 v[4:5], v[6:7], off offset:1136
	s_barrier
	s_cbranch_scc1 .LBB0_628

; __device__ __forceinline__ void phase_prologue(KArgs args, LAS unsigned char* lds, int G, int bid, int tid, int wave, int lane) {
;     ...
;     if (bid < 8) { const int pair = bid, L = pair >> 1, kv = pair & 1, j = tid & 255, half = tid >> 8;
;         const float* pe = (kv ? args->in[I_PEV] : args->in[I_PEK]) + L * 2048 + 1024 * half; const float* w1 = (kv ? args->in[I_WV1] : args->in[I_WK1]) + ((size_t)L * 2048 + 1024 * half) * 256 + j;
;         float s0 = 0.f, s1 = 0.f, s2 = 0.f, s3 = 0.f;
; #pragma unroll 4
;         for (int k = 0; k < 1024; k += 4) { s0 += pe[k] * w1[(size_t)k * 256]; s1 += pe[k + 1] * w1[(size_t)(k + 1) * 256]; s2 += pe[k + 2] * w1[(size_t)(k + 2) * 256]; s3 += pe[k + 3] * w1[(size_t)(k + 3) * 256]; }
.LBB0_1385:
	s_or_b64 exec, exec, s[6:7]
	s_cmp_lt_i32 s29, 8
	s_cbranch_scc0 .LBB0_1393
	s_ashr_i32 s6, s29, 1
	s_lshl_b32 s4, s6, 11
	s_and_b32 s7, s29, 1
	s_ashr_i32 s5, s4, 31
	s_cmp_eq_u32 s7, 0
	s_cselect_b64 s[8:9], -1, 0
	s_movk_i32 s7, 0x58
	s_and_b64 s[10:11], s[8:9], exec
	s_cselect_b32 s12, s7, 0x60
	s_movk_i32 s7, 0x68
	s_cselect_b32 s14, s7, 0x88
	s_ashr_i32 s7, s6, 31
	s_lshl_b64 s[10:11], s[6:7], 21
	s_add_u32 s12, s0, s12
	s_addc_u32 s13, s1, 0
	s_add_u32 s14, s0, s14
	s_addc_u32 s15, s1, 0
	s_load_dwordx2 s[16:17], s[12:13], 0x0
	s_load_dwordx2 s[18:19], s[14:15], 0x0
	s_waitcnt vmcnt(0)
	v_and_b32_e32 v4, 0xfffffc00, v72
	v_ashrrev_i32_e32 v5, 31, v4
	s_lshl_b64 s[4:5], s[4:5], 2
	v_lshlrev_b64 v[2:3], 10, v[4:5]
	s_waitcnt lgkmcnt(0)
	s_add_u32 s4, s16, s4
	v_and_b32_e32 v1, 0xff, v67
	v_lshl_add_u64 v[2:3], s[10:11], 0, v[2:3]
	s_addc_u32 s5, s17, s5
	v_lshl_or_b32 v2, v1, 2, v2
	v_lshl_add_u64 v[4:5], v[4:5], 2, s[4:5]
	v_lshl_add_u64 v[2:3], s[18:19], 0, v[2:3]
	s_mov_b64 s[10:11], 0x3c00
	v_lshl_add_u64 v[6:7], v[4:5], 0, 32
	v_mov_b32_e32 v4, 0
	v_lshl_add_u64 v[2:3], v[2:3], 0, s[10:11]
	s_mov_b32 s7, -4
	s_movk_i32 s12, 0xe000
	s_movk_i32 s13, 0xf000
	s_mov_b64 s[10:11], 0x10000
	v_mov_b32_e32 v5, v4
	v_mov_b32_e32 v8, v4
	v_mov_b32_e32 v9, v4
	s_mov_b64 s[4:5], 0x100
.Lpro_dot:
	v_add_co_u32_e32 v196, vcc, 0xffffd000, v2
	s_nop 1
	v_addc_co_u32_e32 v197, vcc, -1, v3, vcc
	v_add_co_u32_e32 v198, vcc, 0xffffe000, v2
	s_nop 1
	v_addc_co_u32_e32 v199, vcc, -1, v3, vcc
	v_add_co_u32_e32 v200, vcc, 0xfffff000, v2
	s_nop 1
	v_addc_co_u32_e32 v201, vcc, -1, v3, vcc
	v_add_co_u32_e32 v204, vcc, 0x1000, v2
	s_nop 1
	v_addc_co_u32_e32 v205, vcc, 0, v3, vcc
	v_add_co_u32_e32 v206, vcc, 0x2000, v2
	s_nop 1
	v_addc_co_u32_e32 v207, vcc, 0, v3, vcc
	v_add_co_u32_e32 v208, vcc, 0x3000, v2
	s_nop 1
	v_addc_co_u32_e32 v209, vcc, 0, v3, vcc
	v_add_co_u32_e32 v210, vcc, 0x4000, v2
	s_nop 1
	v_addc_co_u32_e32 v211, vcc, 0, v3, vcc
	v_add_co_u32_e32 v212, vcc, 0x5000, v2
	s_nop 1
	v_addc_co_u32_e32 v213, vcc, 0, v3, vcc
	v_add_co_u32_e32 v214, vcc, 0x6000, v2
	s_nop 1
	v_addc_co_u32_e32 v215, vcc, 0, v3, vcc
	v_add_co_u32_e32 v216, vcc, 0x7000, v2
	s_nop 1
	v_addc_co_u32_e32 v217, vcc, 0, v3, vcc
	v_add_co_u32_e32 v218, vcc, 0x8000, v2
	s_nop 1
	v_addc_co_u32_e32 v219, vcc, 0, v3, vcc
	v_add_co_u32_e32 v220, vcc, 0x9000, v2
	s_nop 1
	v_addc_co_u32_e32 v221, vcc, 0, v3, vcc
	v_add_co_u32_e32 v222, vcc, 0xa000, v2
	s_nop 1
	v_addc_co_u32_e32 v223, vcc, 0, v3, vcc
	v_add_co_u32_e32 v224, vcc, 0xb000, v2
	s_nop 1
	v_addc_co_u32_e32 v225, vcc, 0, v3, vcc
	v_add_co_u32_e32 v226, vcc, 0xc000, v2
	s_nop 1
	v_addc_co_u32_e32 v227, vcc, 0, v3, vcc
	global_load_dwordx4 v[68:71], v[6:7], off offset:-32
	global_load_dwordx4 v[72:75], v[6:7], off offset:-16
	global_load_dwordx4 v[76:79], v[6:7], off
	global_load_dwordx4 v[80:83], v[6:7], off offset:16
	global_load_dword v132, v[196:197], off offset:-3072
	global_load_dword v133, v[196:197], off offset:-2048
	global_load_dword v134, v[196:197], off offset:-1024
	global_load_dword v135, v[196:197], off
	global_load_dword v136, v[198:199], off offset:-3072
	global_load_dword v137, v[198:199], off offset:-2048
	global_load_dword v138, v[198:199], off offset:-1024
	global_load_dword v139, v[198:199], off
	global_load_dword v140, v[200:201], off offset:-3072
	global_load_dword v141, v[200:201], off offset:-2048
	global_load_dword v142, v[200:201], off offset:-1024
	global_load_dword v143, v[200:201], off
	global_load_dword v144, v[2:3], off offset:-3072
	global_load_dword v145, v[2:3], off offset:-2048
	global_load_dword v146, v[2:3], off offset:-1024
	global_load_dword v147, v[2:3], off
	global_load_dwordx4 v[84:87], v[6:7], off offset:32
	global_load_dwordx4 v[88:91], v[6:7], off offset:48
	global_load_dwordx4 v[92:95], v[6:7], off offset:64
	global_load_dwordx4 v[96:99], v[6:7], off offset:80
	global_load_dword v148, v[204:205], off offset:-3072
	global_load_dword v149, v[204:205], off offset:-2048
	global_load_dword v150, v[204:205], off offset:-1024
	global_load_dword v151, v[204:205], off
	global_load_dword v152, v[206:207], off offset:-3072
	global_load_dword v153, v[206:207], off offset:-2048
	global_load_dword v154, v[206:207], off offset:-1024
	global_load_dword v155, v[206:207], off
	global_load_dword v156, v[208:209], off offset:-3072
	global_load_dword v157, v[208:209], off offset:-2048
	global_load_dword v158, v[208:209], off offset:-1024
	global_load_dword v159, v[208:209], off
	global_load_dword v160, v[210:211], off offset:-3072
	global_load_dword v161, v[210:211], off offset:-2048
	global_load_dword v162, v[210:211], off offset:-1024
	global_load_dword v163, v[210:211], off
	global_load_dwordx4 v[100:103], v[6:7], off offset:96
	global_load_dwordx4 v[104:107], v[6:7], off offset:112
	global_load_dwordx4 v[108:111], v[6:7], off offset:128
	global_load_dwordx4 v[112:115], v[6:7], off offset:144
	global_load_dword v164, v[212:213], off offset:-3072
	global_load_dword v165, v[212:213], off offset:-2048
	global_load_dword v166, v[212:213], off offset:-1024
	global_load_dword v167, v[212:213], off
	global_load_dword v168, v[214:215], off offset:-3072
	global_load_dword v169, v[214:215], off offset:-2048
	global_load_dword v170, v[214:215], off offset:-1024
	global_load_dword v171, v[214:215], off
	global_load_dword v172, v[216:217], off offset:-3072
	global_load_dword v173, v[216:217], off offset:-2048
	global_load_dword v174, v[216:217], off offset:-1024
	global_load_dword v175, v[216:217], off
	global_load_dword v176, v[218:219], off offset:-3072
	global_load_dword v177, v[218:219], off offset:-2048
	global_load_dword v178, v[218:219], off offset:-1024
	global_load_dword v179, v[218:219], off
	global_load_dwordx4 v[116:119], v[6:7], off offset:160
	global_load_dwordx4 v[120:123], v[6:7], off offset:176
	global_load_dwordx4 v[124:127], v[6:7], off offset:192
	global_load_dwordx4 v[128:131], v[6:7], off offset:208
	global_load_dword v180, v[220:221], off offset:-3072
	global_load_dword v181, v[220:221], off offset:-2048
	global_load_dword v182, v[220:221], off offset:-1024
	global_load_dword v183, v[220:221], off
	global_load_dword v184, v[222:223], off offset:-3072
	global_load_dword v185, v[222:223], off offset:-2048
	global_load_dword v186, v[222:223], off offset:-1024
	global_load_dword v187, v[222:223], off
	global_load_dword v188, v[224:225], off offset:-3072
	global_load_dword v189, v[224:225], off offset:-2048
	global_load_dword v190, v[224:225], off offset:-1024
	global_load_dword v191, v[224:225], off
	global_load_dword v192, v[226:227], off offset:-3072
	global_load_dword v193, v[226:227], off offset:-2048
	global_load_dword v194, v[226:227], off offset:-1024
	global_load_dword v195, v[226:227], off
	s_add_i32 s7, s7, 64
	v_lshl_add_u64 v[6:7], v[6:7], 0, s[4:5]
	v_lshl_add_u64 v[2:3], v[2:3], 0, s[10:11]
	s_cmpk_gt_u32 s7, 0x3fb
	s_waitcnt vmcnt(60)
; #define LAS __attribute__((address_space(3)))
; __device__ __forceinline__ void phase_prologue(KArgs args, LAS unsigned char* lds, int G, int bid, int tid, int wave, int lane) {
;     ...
;         float s0 = 0.f, s1 = 0.f, s2 = 0.f, s3 = 0.f;
; #pragma unroll 4
;         for (int k = 0; k < 1024; k += 4) { s0 += pe[k] * w1[(size_t)k * 256]; s1 += pe[k + 1] * w1[(size_t)(k + 1) * 256]; s2 += pe[k + 2] * w1[(size_t)(k + 2) * 256]; s3 += pe[k + 3] * w1[(size_t)(k + 3) * 256]; }
;         LAS float* red = (LAS float*)(lds + 8 * 16384);
;         if (half) red[j] = (s0 + s1) + (s2 + s3);
;         __syncthreads();
;         if (!half) ((float*)(ws + WS_BK1))[pair * 256 + j] = (kv ? args->in[I_BV1] : args->in[I_BK1])[L * 256 + j] + ((s0 + s1) + (s2 + s3)) + red[j]; }
	v_pk_fma_f32 v[4:5], v[68:69], v[132:133], v[4:5]
	v_pk_fma_f32 v[8:9], v[70:71], v[134:135], v[8:9]
	v_pk_fma_f32 v[4:5], v[72:73], v[136:137], v[4:5]
	v_pk_fma_f32 v[8:9], v[74:75], v[138:139], v[8:9]
	v_pk_fma_f32 v[4:5], v[76:77], v[140:141], v[4:5]
	v_pk_fma_f32 v[8:9], v[78:79], v[142:143], v[8:9]
	v_pk_fma_f32 v[4:5], v[80:81], v[144:145], v[4:5]
	v_pk_fma_f32 v[8:9], v[82:83], v[146:147], v[8:9]
	s_waitcnt vmcnt(40)
	v_pk_fma_f32 v[4:5], v[84:85], v[148:149], v[4:5]
	v_pk_fma_f32 v[8:9], v[86:87], v[150:151], v[8:9]
	v_pk_fma_f32 v[4:5], v[88:89], v[152:153], v[4:5]
	v_pk_fma_f32 v[8:9], v[90:91], v[154:155], v[8:9]
	v_pk_fma_f32 v[4:5], v[92:93], v[156:157], v[4:5]
	v_pk_fma_f32 v[8:9], v[94:95], v[158:159], v[8:9]
	v_pk_fma_f32 v[4:5], v[96:97], v[160:161], v[4:5]
	v_pk_fma_f32 v[8:9], v[98:99], v[162:163], v[8:9]
	s_waitcnt vmcnt(20)
	v_pk_fma_f32 v[4:5], v[100:101], v[164:165], v[4:5]
	v_pk_fma_f32 v[8:9], v[102:103], v[166:167], v[8:9]
	v_pk_fma_f32 v[4:5], v[104:105], v[168:169], v[4:5]
	v_pk_fma_f32 v[8:9], v[106:107], v[170:171], v[8:9]
	v_pk_fma_f32 v[4:5], v[108:109], v[172:173], v[4:5]
	v_pk_fma_f32 v[8:9], v[110:111], v[174:175], v[8:9]
	v_pk_fma_f32 v[4:5], v[112:113], v[176:177], v[4:5]
	v_pk_fma_f32 v[8:9], v[114:115], v[178:179], v[8:9]
	s_waitcnt vmcnt(0)
	v_pk_fma_f32 v[4:5], v[116:117], v[180:181], v[4:5]
	v_pk_fma_f32 v[8:9], v[118:119], v[182:183], v[8:9]
	v_pk_fma_f32 v[4:5], v[120:121], v[184:185], v[4:5]
	v_pk_fma_f32 v[8:9], v[122:123], v[186:187], v[8:9]
	v_pk_fma_f32 v[4:5], v[124:125], v[188:189], v[4:5]
	v_pk_fma_f32 v[8:9], v[126:127], v[190:191], v[8:9]
	v_pk_fma_f32 v[4:5], v[128:129], v[192:193], v[4:5]
	v_pk_fma_f32 v[8:9], v[130:131], v[194:195], v[8:9]
	s_cbranch_scc0 .Lpro_dot
	s_movk_i32 s4, 0x100
	v_cmp_gt_u32_e32 vcc, s4, v67
	s_movk_i32 s4, 0xff
	s_add_i32 s7, 0, 0x20000
	v_add_f32_e32 v4, v4, v5
	v_add_f32_e32 v5, v8, v9
	v_cmp_lt_u32_e64 s[4:5], s4, v67
	v_lshl_add_u32 v2, v1, 2, s7
	v_add_f32_e32 v1, v4, v5
	s_and_saveexec_b64 s[10:11], s[4:5]
	ds_write_b32 v2, v1
	s_or_b64 exec, exec, s[10:11]
	s_waitcnt lgkmcnt(0)
	s_barrier
	s_and_saveexec_b64 s[4:5], vcc
	s_cbranch_execz .LBB0_1392
	s_movk_i32 s7, 0x70
	s_and_b64 s[8:9], s[8:9], exec
	s_cselect_b32 s7, s7, 0x90
	s_lshl_b32 s8, s29, 8
	s_add_u32 s0, s0, s7
	s_addc_u32 s1, s1, 0
	s_load_dwordx2 s[0:1], s[0:1], 0x0
	v_lshl_add_u32 v4, s6, 8, v67
	v_ashrrev_i32_e32 v5, 31, v4
	s_waitcnt lgkmcnt(0)
	v_lshl_add_u64 v[4:5], v[4:5], 2, s[0:1]
	global_load_dword v4, v[4:5], off
	ds_read_b32 v5, v2
	v_subrev_u32_e32 v2, s8, v0
	v_ashrrev_i32_e32 v3, 31, v2
	v_lshl_add_u64 v[2:3], v[2:3], 2, s[2:3]
	v_add_co_u32_e32 v0, vcc, 0x100000, v2
	s_waitcnt vmcnt(0)
	v_add_f32_e32 v1, v1, v4
	s_waitcnt lgkmcnt(0)
	v_add_f32_e32 v2, v1, v5
	v_addc_co_u32_e32 v1, vcc, 0, v3, vcc
	global_store_dword v[0:1], v2, off
